# speedup vs baseline: 1.0408x; 1.0153x over previous
.LBB0_4:
	s_or_b64 exec, exec, s[4:5]
	s_cmp_eq_u32 s94, 0
	s_cbranch_scc1 .LBB0_64
	s_add_i32 s85, s85, 1
	v_min_i32_e32 v21, s40, v20
	v_lshl_add_u32 v21, v21, 12, v17
	global_load_dwordx4 v[86:89], v21, s[38:39] nt
	v_add_u32_e32 v22, 4, v20
	v_min_i32_e32 v22, s40, v22
	v_lshl_add_u32 v22, v22, 12, v17
	global_load_dwordx4 v[74:77], v22, s[38:39] nt
	v_add_u32_e32 v21, 8, v20
	v_min_i32_e32 v21, s40, v21
	v_lshl_add_u32 v21, v21, 12, v17
	global_load_dwordx4 v[78:81], v21, s[38:39] nt
	v_add_u32_e32 v22, 12, v20
	v_min_i32_e32 v22, s40, v22
	v_lshl_add_u32 v22, v22, 12, v17
	global_load_dwordx4 v[58:61], v22, s[38:39] nt
	v_add_u32_e32 v21, 16, v20
	v_min_i32_e32 v21, s40, v21
	v_lshl_add_u32 v21, v21, 12, v17
	global_load_dwordx4 v[62:65], v21, s[38:39] nt
	v_add_u32_e32 v22, 20, v20
	v_min_i32_e32 v22, s40, v22
	v_lshl_add_u32 v22, v22, 12, v17
	global_load_dwordx4 v[50:53], v22, s[38:39] nt
	v_add_u32_e32 v21, 24, v20
	v_min_i32_e32 v21, s40, v21
	v_lshl_add_u32 v21, v21, 12, v17
	global_load_dwordx4 v[54:57], v21, s[38:39] nt
	v_add_u32_e32 v22, 28, v20
	v_min_i32_e32 v22, s40, v22
	v_lshl_add_u32 v22, v22, 12, v17
	global_load_dwordx4 v[178:181], v22, s[38:39] nt
	s_mov_b64 s[4:5], 0
	s_waitcnt lgkmcnt(0)
	s_barrier

.LBB0_48:
	s_cmp_eq_u32 s94, 0
	s_cbranch_scc1 .Lno_next
	s_lshl_b32 s44, s92, 12
	s_lshl_b32 s45, s91, 8
	s_add_u32 s44, s44, s45
	s_add_u32 s34, s70, s44
	s_addc_u32 s35, s71, 0
	s_add_u32 s36, s74, s44
	s_addc_u32 s37, s75, 0
	s_add_u32 s38, s68, s44
	s_addc_u32 s39, s69, 0
	s_add_i32 s40, s93, -1
	s_cmp_gt_i32 s94, 1
	s_cselect_b32 s41, 64, 0
	s_add_i32 s42, s94, -1
	s_min_i32 s42, s42, 2
	s_lshl_b32 s42, s42, 6
	s_add_i32 s43, s89, s33
	v_lshrrev_b32_e32 v16, 4, v0
	v_and_b32_e32 v17, 15, v0
	v_lshlrev_b32_e32 v17, 4, v17
	v_bfe_u32 v20, v0, 4, 2
	v_add_u32_e32 v20, s43, v20
	v_min_i32_e32 v18, s40, v16
	v_lshl_add_u32 v18, v18, 12, v17
	global_load_dwordx4 v[70:73], v18, s[34:35]
	v_add_u32_e32 v19, 32, v16
	v_min_i32_e32 v19, s40, v19
	v_lshl_add_u32 v19, v19, 12, v17
	global_load_dwordx4 v[66:69], v19, s[34:35]
	global_load_dwordx4 v[182:185], v18, s[36:37]
	global_load_dwordx4 v[186:189], v19, s[36:37]
	v_add_u32_e32 v21, s41, v16
	v_min_i32_e32 v21, s40, v21
	v_lshl_add_u32 v21, v21, 12, v17
	global_load_dwordx4 v[90:93], v21, s[34:35]
	v_add3_u32 v22, s41, v16, 32
	v_min_i32_e32 v22, s40, v22
	v_lshl_add_u32 v22, v22, 12, v17
	global_load_dwordx4 v[82:85], v22, s[34:35]
	v_add_u32_e32 v18, s42, v16
	v_min_i32_e32 v18, s40, v18
	v_lshl_add_u32 v18, v18, 12, v17
	global_load_dwordx4 v[98:101], v18, s[34:35]
	v_add3_u32 v19, s42, v16, 32
	v_min_i32_e32 v19, s40, v19
	v_lshl_add_u32 v19, v19, 12, v17
	global_load_dwordx4 v[94:97], v19, s[34:35]
